# grid barrier: non-last arrivers issue the acquire's L1 invalidate on arrival (overlapped with the wait) instead of after the release
# speedup vs baseline: 1.0243x; 1.0243x over previous
; __device__ __forceinline__ unsigned xb_ld(unsigned* p)              { unsigned GAS* g = (unsigned GAS*)p; asm volatile("" : "+s"(g)); return __hip_atomic_load(g, __ATOMIC_RELAXED, __HIP_MEMORY_SCOPE_AGENT); }
; __device__ __forceinline__ unsigned xb_add(unsigned* p, unsigned v) { unsigned GAS* g = (unsigned GAS*)p; asm volatile("" : "+s"(g)); return __hip_atomic_fetch_add(g, v, __ATOMIC_RELAXED, __HIP_MEMORY_SCOPE_AGENT); }
; #define XB_SPIN(cond, bar) do { unsigned _sp = 0; while (cond) { __builtin_amdgcn_s_sleep(1); \
;     if ((++_sp & 255u) == 0u) { if (xb_ld(&(bar)[XB_TMO])) break; if (_sp > XB_SPIN_CAP) { (void)xb_add(&(bar)[XB_TMO], 1u); break; } } } } while (0)
; __device__ __forceinline__ void xcd_barrier(const XcdBarrier& b) {
;     ...
;         unsigned nloc = b.st[0], nx = b.st[1];
;         if (nloc == 0u) { xcd_barrier_complete(bar, b.x, nloc, nx); b.st[0] = nloc; b.st[1] = nx; }
;         const unsigned old = xb_add(&bar[XB_XSUB(b.x)], 1u);
;         const unsigned gen = old / nloc;
;         if (old + 1u == (gen + 1u) * nloc) {
;     ...
;         } else {
;             XB_SPIN(xb_ld(&bar[XB_XGEN(b.x)]) == gen, bar);
;             __builtin_amdgcn_fence(__ATOMIC_ACQUIRE, "agent");
;             asm volatile("s_waitcnt vmcnt(0)" ::: "memory");
.LBB0_174:
	s_or_b64 exec, exec, s[10:11]
	v_cvt_f32_u32_e32 v5, v3
	s_waitcnt vmcnt(0)
	v_readfirstlane_b32 s6, v4
	s_mov_b32 s30, 1
	v_rcp_iflag_f32_e32 v5, v5
	v_add_u32_e32 v6, s6, v2
	v_mul_f32_e32 v4, 0x4f7ffffe, v5
	v_cvt_u32_f32_e32 v4, v4
	v_sub_u32_e32 v5, 0, v3
	v_mul_lo_u32 v2, v5, v4
	v_mul_hi_u32 v2, v4, v2
	v_add_u32_e32 v2, v4, v2
	v_mul_hi_u32 v2, v6, v2
	v_mul_lo_u32 v4, v2, v3
	v_sub_u32_e32 v4, v6, v4
	v_add_u32_e32 v5, 1, v2
	v_cmp_ge_u32_e32 vcc, v4, v3
	s_nop 1
	v_cndmask_b32_e32 v2, v2, v5, vcc
	v_sub_u32_e32 v5, v4, v3
	v_cndmask_b32_e32 v4, v4, v5, vcc
	v_add_u32_e32 v5, 1, v2
	v_cmp_ge_u32_e32 vcc, v4, v3
	v_add_u32_e32 v4, 1, v6
	s_nop 0
	v_cndmask_b32_e32 v2, v2, v5, vcc
	v_mul_lo_u32 v5, v3, v2
	v_add_u32_e32 v3, v5, v3
	v_cmp_ne_u32_e32 vcc, v4, v3
	s_and_saveexec_b64 s[6:7], vcc
	s_xor_b64 s[6:7], exec, s[6:7]
	s_cbranch_execz .LBB0_190
	buffer_inv sc1
	s_add_u32 s8, s4, 0x200
	s_addc_u32 s9, s5, 0
	s_add_u32 s10, s28, 0x2400
	s_addc_u32 s11, s29, 0
	s_mov_b64 s[12:13], 0
	s_waitcnt lgkmcnt(0)
	v_mov_b32_e32 v1, 0
	s_branch .LBB0_178

; __device__ __forceinline__ unsigned xb_ld(unsigned* p)              { unsigned GAS* g = (unsigned GAS*)p; asm volatile("" : "+s"(g)); return __hip_atomic_load(g, __ATOMIC_RELAXED, __HIP_MEMORY_SCOPE_AGENT); }
; #define XB_SPIN(cond, bar) do { unsigned _sp = 0; while (cond) { __builtin_amdgcn_s_sleep(1); \
;     if ((++_sp & 255u) == 0u) { if (xb_ld(&(bar)[XB_TMO])) break; if (_sp > XB_SPIN_CAP) { (void)xb_add(&(bar)[XB_TMO], 1u); break; } } } } while (0)
; __device__ __forceinline__ void xcd_barrier(const XcdBarrier& b) {
;     ...
;             XB_SPIN(xb_ld(&bar[XB_XGEN(b.x)]) == gen, bar);
;             __builtin_amdgcn_fence(__ATOMIC_ACQUIRE, "agent");
;             asm volatile("s_waitcnt vmcnt(0)" ::: "memory");
.LBB0_189:
	s_or_b64 exec, exec, s[10:11]
	s_waitcnt vmcnt(0)
	s_waitcnt vmcnt(0)

; __device__ __forceinline__ unsigned xb_ld(unsigned* p)              { unsigned GAS* g = (unsigned GAS*)p; asm volatile("" : "+s"(g)); return __hip_atomic_load(g, __ATOMIC_RELAXED, __HIP_MEMORY_SCOPE_AGENT); }
; __device__ __forceinline__ unsigned xb_add(unsigned* p, unsigned v) { unsigned GAS* g = (unsigned GAS*)p; asm volatile("" : "+s"(g)); return __hip_atomic_fetch_add(g, v, __ATOMIC_RELAXED, __HIP_MEMORY_SCOPE_AGENT); }
; #define XB_SPIN(cond, bar) do { unsigned _sp = 0; while (cond) { __builtin_amdgcn_s_sleep(1); \
;     if ((++_sp & 255u) == 0u) { if (xb_ld(&(bar)[XB_TMO])) break; if (_sp > XB_SPIN_CAP) { (void)xb_add(&(bar)[XB_TMO], 1u); break; } } } } while (0)
; __device__ __forceinline__ void xcd_barrier(const XcdBarrier& b) {
;     ...
;         unsigned nloc = b.st[0], nx = b.st[1];
;         if (nloc == 0u) { xcd_barrier_complete(bar, b.x, nloc, nx); b.st[0] = nloc; b.st[1] = nx; }
;         const unsigned old = xb_add(&bar[XB_XSUB(b.x)], 1u);
;         const unsigned gen = old / nloc;
;         if (old + 1u == (gen + 1u) * nloc) {
;     ...
;         } else {
;             XB_SPIN(xb_ld(&bar[XB_XGEN(b.x)]) == gen, bar);
;             __builtin_amdgcn_fence(__ATOMIC_ACQUIRE, "agent");
;             asm volatile("s_waitcnt vmcnt(0)" ::: "memory");
.LBB0_251:
	s_or_b64 exec, exec, s[8:9]
	v_cvt_f32_u32_e32 v5, v3
	s_waitcnt vmcnt(0)
	v_readfirstlane_b32 s4, v4
	s_mov_b32 s28, 1
	v_rcp_iflag_f32_e32 v5, v5
	v_add_u32_e32 v6, s4, v2
	v_mul_f32_e32 v4, 0x4f7ffffe, v5
	v_cvt_u32_f32_e32 v4, v4
	v_sub_u32_e32 v5, 0, v3
	v_mul_lo_u32 v2, v5, v4
	v_mul_hi_u32 v2, v4, v2
	v_add_u32_e32 v2, v4, v2
	v_mul_hi_u32 v2, v6, v2
	v_mul_lo_u32 v4, v2, v3
	v_sub_u32_e32 v4, v6, v4
	v_add_u32_e32 v5, 1, v2
	v_cmp_ge_u32_e32 vcc, v4, v3
	s_nop 1
	v_cndmask_b32_e32 v2, v2, v5, vcc
	v_sub_u32_e32 v5, v4, v3
	v_cndmask_b32_e32 v4, v4, v5, vcc
	v_add_u32_e32 v5, 1, v2
	v_cmp_ge_u32_e32 vcc, v4, v3
	v_add_u32_e32 v4, 1, v6
	s_nop 0
	v_cndmask_b32_e32 v2, v2, v5, vcc
	v_mul_lo_u32 v5, v3, v2
	v_add_u32_e32 v3, v5, v3
	v_cmp_ne_u32_e32 vcc, v4, v3
	s_and_saveexec_b64 s[4:5], vcc
	s_xor_b64 s[4:5], exec, s[4:5]
	s_cbranch_execz .LBB0_267
	buffer_inv sc1
	s_add_u32 s6, s2, 0x200
	s_addc_u32 s7, s3, 0
	s_add_u32 s8, s26, 0x2400
	s_addc_u32 s9, s27, 0
	s_mov_b64 s[10:11], 0
	s_waitcnt lgkmcnt(0)
	v_mov_b32_e32 v1, 0
	s_branch .LBB0_255

; __device__ __forceinline__ unsigned xb_ld(unsigned* p)              { unsigned GAS* g = (unsigned GAS*)p; asm volatile("" : "+s"(g)); return __hip_atomic_load(g, __ATOMIC_RELAXED, __HIP_MEMORY_SCOPE_AGENT); }
; #define XB_SPIN(cond, bar) do { unsigned _sp = 0; while (cond) { __builtin_amdgcn_s_sleep(1); \
;     if ((++_sp & 255u) == 0u) { if (xb_ld(&(bar)[XB_TMO])) break; if (_sp > XB_SPIN_CAP) { (void)xb_add(&(bar)[XB_TMO], 1u); break; } } } } while (0)
; __device__ __forceinline__ void xcd_barrier(const XcdBarrier& b) {
;     ...
;             XB_SPIN(xb_ld(&bar[XB_XGEN(b.x)]) == gen, bar);
;             __builtin_amdgcn_fence(__ATOMIC_ACQUIRE, "agent");
;             asm volatile("s_waitcnt vmcnt(0)" ::: "memory");
.LBB0_266:
	s_or_b64 exec, exec, s[8:9]
	s_waitcnt vmcnt(0)
	s_waitcnt vmcnt(0)

; __device__ __forceinline__ unsigned xb_ld(unsigned* p)              { unsigned GAS* g = (unsigned GAS*)p; asm volatile("" : "+s"(g)); return __hip_atomic_load(g, __ATOMIC_RELAXED, __HIP_MEMORY_SCOPE_AGENT); }
; __device__ __forceinline__ unsigned xb_add(unsigned* p, unsigned v) { unsigned GAS* g = (unsigned GAS*)p; asm volatile("" : "+s"(g)); return __hip_atomic_fetch_add(g, v, __ATOMIC_RELAXED, __HIP_MEMORY_SCOPE_AGENT); }
; #define XB_SPIN(cond, bar) do { unsigned _sp = 0; while (cond) { __builtin_amdgcn_s_sleep(1); \
;     if ((++_sp & 255u) == 0u) { if (xb_ld(&(bar)[XB_TMO])) break; if (_sp > XB_SPIN_CAP) { (void)xb_add(&(bar)[XB_TMO], 1u); break; } } } } while (0)
; __device__ __forceinline__ void xcd_barrier(const XcdBarrier& b) {
;     ...
;         unsigned nloc = b.st[0], nx = b.st[1];
;         if (nloc == 0u) { xcd_barrier_complete(bar, b.x, nloc, nx); b.st[0] = nloc; b.st[1] = nx; }
;         const unsigned old = xb_add(&bar[XB_XSUB(b.x)], 1u);
;         const unsigned gen = old / nloc;
;         if (old + 1u == (gen + 1u) * nloc) {
;     ...
;         } else {
;             XB_SPIN(xb_ld(&bar[XB_XGEN(b.x)]) == gen, bar);
;             __builtin_amdgcn_fence(__ATOMIC_ACQUIRE, "agent");
;             asm volatile("s_waitcnt vmcnt(0)" ::: "memory");
.LBB0_447:
	s_or_b64 exec, exec, s[8:9]
	v_cvt_f32_u32_e32 v6, v4
	s_waitcnt vmcnt(0)
	v_readfirstlane_b32 s4, v5
	v_sub_u32_e32 v5, 0, v4
	v_rcp_iflag_f32_e32 v6, v6
	v_add_u32_e32 v7, s4, v2
	v_mul_f32_e32 v6, 0x4f7ffffe, v6
	v_cvt_u32_f32_e32 v6, v6
	v_mul_lo_u32 v2, v5, v6
	v_mul_hi_u32 v2, v6, v2
	v_add_u32_e32 v2, v6, v2
	v_mul_hi_u32 v2, v7, v2
	v_mul_lo_u32 v5, v2, v4
	v_sub_u32_e32 v5, v7, v5
	v_add_u32_e32 v6, 1, v2
	v_cmp_ge_u32_e32 vcc, v5, v4
	s_nop 1
	v_cndmask_b32_e32 v2, v2, v6, vcc
	v_sub_u32_e32 v6, v5, v4
	v_cndmask_b32_e32 v5, v5, v6, vcc
	v_add_u32_e32 v6, 1, v2
	v_cmp_ge_u32_e32 vcc, v5, v4
	v_add_u32_e32 v5, 1, v7
	s_nop 0
	v_cndmask_b32_e32 v2, v2, v6, vcc
	v_mul_lo_u32 v6, v4, v2
	v_add_u32_e32 v4, v6, v4
	v_cmp_ne_u32_e32 vcc, v5, v4
	s_and_saveexec_b64 s[4:5], vcc
	s_xor_b64 s[4:5], exec, s[4:5]
	s_cbranch_execz .LBB0_463
	buffer_inv sc1
	s_add_u32 s6, s2, 0x200
	s_addc_u32 s7, s3, 0
	s_add_u32 s8, s27, 0x2400
	s_addc_u32 s9, s28, 0
	s_mov_b32 s29, 1
	s_mov_b64 s[10:11], 0
	s_branch .LBB0_451

; __device__ __forceinline__ unsigned xb_ld(unsigned* p)              { unsigned GAS* g = (unsigned GAS*)p; asm volatile("" : "+s"(g)); return __hip_atomic_load(g, __ATOMIC_RELAXED, __HIP_MEMORY_SCOPE_AGENT); }
; __device__ __forceinline__ unsigned xb_add(unsigned* p, unsigned v) { unsigned GAS* g = (unsigned GAS*)p; asm volatile("" : "+s"(g)); return __hip_atomic_fetch_add(g, v, __ATOMIC_RELAXED, __HIP_MEMORY_SCOPE_AGENT); }
; #define XB_SPIN(cond, bar) do { unsigned _sp = 0; while (cond) { __builtin_amdgcn_s_sleep(1); \
;     if ((++_sp & 255u) == 0u) { if (xb_ld(&(bar)[XB_TMO])) break; if (_sp > XB_SPIN_CAP) { (void)xb_add(&(bar)[XB_TMO], 1u); break; } } } } while (0)
; __device__ __forceinline__ void xcd_barrier(const XcdBarrier& b) {
;     ...
;         unsigned nloc = b.st[0], nx = b.st[1];
;         if (nloc == 0u) { xcd_barrier_complete(bar, b.x, nloc, nx); b.st[0] = nloc; b.st[1] = nx; }
;         const unsigned old = xb_add(&bar[XB_XSUB(b.x)], 1u);
;         const unsigned gen = old / nloc;
;         if (old + 1u == (gen + 1u) * nloc) {
;     ...
;         } else {
;             XB_SPIN(xb_ld(&bar[XB_XGEN(b.x)]) == gen, bar);
;             __builtin_amdgcn_fence(__ATOMIC_ACQUIRE, "agent");
;             asm volatile("s_waitcnt vmcnt(0)" ::: "memory");
.LBB0_1444:
	s_or_b64 exec, exec, s[10:11]
	v_cvt_f32_u32_e32 v6, v4
	s_waitcnt vmcnt(0)
	v_readfirstlane_b32 s4, v5
	v_sub_u32_e32 v5, 0, v4
	v_rcp_iflag_f32_e32 v6, v6
	v_add_u32_e32 v7, s4, v2
	v_mul_f32_e32 v6, 0x4f7ffffe, v6
	v_cvt_u32_f32_e32 v6, v6
	v_mul_lo_u32 v2, v5, v6
	v_mul_hi_u32 v2, v6, v2
	v_add_u32_e32 v2, v6, v2
	v_mul_hi_u32 v2, v7, v2
	v_mul_lo_u32 v5, v2, v4
	v_sub_u32_e32 v5, v7, v5
	v_add_u32_e32 v6, 1, v2
	v_cmp_ge_u32_e32 vcc, v5, v4
	s_nop 1
	v_cndmask_b32_e32 v2, v2, v6, vcc
	v_sub_u32_e32 v6, v5, v4
	v_cndmask_b32_e32 v5, v5, v6, vcc
	v_add_u32_e32 v6, 1, v2
	v_cmp_ge_u32_e32 vcc, v5, v4
	v_add_u32_e32 v5, 1, v7
	s_nop 0
	v_cndmask_b32_e32 v2, v2, v6, vcc
	v_mul_lo_u32 v6, v4, v2
	v_add_u32_e32 v4, v6, v4
	v_cmp_ne_u32_e32 vcc, v5, v4
	s_and_saveexec_b64 s[4:5], vcc
	s_xor_b64 s[4:5], exec, s[4:5]
	s_cbranch_execz .LBB0_1460
	buffer_inv sc1
	s_add_u32 s6, s2, 0x200
	s_addc_u32 s7, s3, 0
	s_add_u32 s10, s29, 0x2400
	s_addc_u32 s11, s30, 0
	s_mov_b32 s31, 1
	s_mov_b64 s[12:13], 0
	s_branch .LBB0_1448

; __device__ __forceinline__ unsigned xb_ld(unsigned* p)              { unsigned GAS* g = (unsigned GAS*)p; asm volatile("" : "+s"(g)); return __hip_atomic_load(g, __ATOMIC_RELAXED, __HIP_MEMORY_SCOPE_AGENT); }
; __device__ __forceinline__ unsigned xb_add(unsigned* p, unsigned v) { unsigned GAS* g = (unsigned GAS*)p; asm volatile("" : "+s"(g)); return __hip_atomic_fetch_add(g, v, __ATOMIC_RELAXED, __HIP_MEMORY_SCOPE_AGENT); }
; #define XB_SPIN(cond, bar) do { unsigned _sp = 0; while (cond) { __builtin_amdgcn_s_sleep(1); \
;     if ((++_sp & 255u) == 0u) { if (xb_ld(&(bar)[XB_TMO])) break; if (_sp > XB_SPIN_CAP) { (void)xb_add(&(bar)[XB_TMO], 1u); break; } } } } while (0)
; __device__ __forceinline__ void xcd_barrier(const XcdBarrier& b) {
;     ...
;         unsigned nloc = b.st[0], nx = b.st[1];
;         if (nloc == 0u) { xcd_barrier_complete(bar, b.x, nloc, nx); b.st[0] = nloc; b.st[1] = nx; }
;         const unsigned old = xb_add(&bar[XB_XSUB(b.x)], 1u);
;         const unsigned gen = old / nloc;
;         if (old + 1u == (gen + 1u) * nloc) {
;     ...
;         } else {
;             XB_SPIN(xb_ld(&bar[XB_XGEN(b.x)]) == gen, bar);
;             __builtin_amdgcn_fence(__ATOMIC_ACQUIRE, "agent");
;             asm volatile("s_waitcnt vmcnt(0)" ::: "memory");
.LBB0_1537:
	s_or_b64 exec, exec, s[8:9]
	v_cvt_f32_u32_e32 v6, v4
	s_waitcnt vmcnt(0)
	v_readfirstlane_b32 s4, v5
	v_sub_u32_e32 v5, 0, v4
	v_rcp_iflag_f32_e32 v6, v6
	v_add_u32_e32 v7, s4, v2
	v_mul_f32_e32 v6, 0x4f7ffffe, v6
	v_cvt_u32_f32_e32 v6, v6
	v_mul_lo_u32 v2, v5, v6
	v_mul_hi_u32 v2, v6, v2
	v_add_u32_e32 v2, v6, v2
	v_mul_hi_u32 v2, v7, v2
	v_mul_lo_u32 v5, v2, v4
	v_sub_u32_e32 v5, v7, v5
	v_add_u32_e32 v6, 1, v2
	v_cmp_ge_u32_e32 vcc, v5, v4
	s_nop 1
	v_cndmask_b32_e32 v2, v2, v6, vcc
	v_sub_u32_e32 v6, v5, v4
	v_cndmask_b32_e32 v5, v5, v6, vcc
	v_add_u32_e32 v6, 1, v2
	v_cmp_ge_u32_e32 vcc, v5, v4
	v_add_u32_e32 v5, 1, v7
	s_nop 0
	v_cndmask_b32_e32 v2, v2, v6, vcc
	v_mul_lo_u32 v6, v4, v2
	v_add_u32_e32 v4, v6, v4
	v_cmp_ne_u32_e32 vcc, v5, v4
	s_and_saveexec_b64 s[4:5], vcc
	s_xor_b64 s[4:5], exec, s[4:5]
	s_cbranch_execz .LBB0_1553
	buffer_inv sc1
	s_add_u32 s6, s2, 0x200
	s_addc_u32 s7, s3, 0
	s_add_u32 s8, s26, 0x2400
	s_addc_u32 s9, s27, 0
	s_mov_b32 s28, 1
	s_mov_b64 s[10:11], 0
	s_branch .LBB0_1541
